# attention loop edge edits: back edge rotated to one taken branch, rescale threshold constant kept in an SGPR, -m block init by moves (on top of the pass C finalize version)
# speedup vs baseline: 1.0009x; 1.0006x over previous
.LBB0_1428:
	s_or_b64 exec, exec, s[10:11]
	v_and_b32_e32 v140, 0xffffffe0, v39
	s_movk_i32 s20, 0xc0
	v_mov_b32_e32 v39, v83
	v_add_u32_e32 v44, 64, v40
	v_mov_b64_e32 v[42:43], s[8:9]
	v_lshl_add_u64 v[38:39], s[8:9], 0, v[38:39]
	v_sub_f32_e32 v46, v18, v159
	v_add_co_u32_e32 v18, vcc, s66, v34
	v_mad_i64_i32 v[44:45], s[8:9], v44, s20, v[42:43]
	v_sub_f32_e32 v47, v19, v159
	v_addc_co_u32_e32 v19, vcc, 0, v35, vcc
	v_lshlrev_b64 v[70:71], 1, v[36:37]
	s_movk_i32 s8, 0x3000
	v_lshl_add_u64 v[36:37], v[44:45], 0, v[70:71]
	global_load_dwordx4 v[56:59], v[18:19], off
	global_load_dwordx4 v[60:63], v[36:37], off
	v_add_co_u32_e32 v18, vcc, s8, v38
	s_movk_i32 s8, 0x6000
	s_nop 0
	v_addc_co_u32_e32 v19, vcc, 0, v39, vcc
	global_load_dwordx4 v[64:67], v[18:19], off
	v_sub_f32_e32 v18, v20, v159
	v_sub_f32_e32 v19, v21, v159
	v_exp_f32_e32 v227, v18
	v_add_co_u32_e32 v18, vcc, s8, v38
	v_exp_f32_e32 v230, v19
	s_nop 0
	v_addc_co_u32_e32 v19, vcc, 0, v39, vcc
	global_load_dwordx4 v[122:125], v[18:19], off
	v_add_u32_e32 v18, 0x80, v40
	v_sub_f32_e32 v20, v22, v159
	v_mad_i64_i32 v[18:19], s[8:9], v18, s20, v[42:43]
	v_sub_f32_e32 v21, v23, v159
	v_exp_f32_e32 v231, v20
	v_lshl_add_u64 v[18:19], v[18:19], 0, v[70:71]
	v_add_co_u32_e32 v20, vcc, s69, v34
	v_exp_f32_e32 v232, v21
	s_nop 0
	v_addc_co_u32_e32 v21, vcc, 0, v35, vcc
	global_load_dwordx4 v[118:121], v[18:19], off
	global_load_dwordx4 v[114:117], v[20:21], off
	v_mad_i64_i32 v[68:69], s[10:11], v40, s20, 0
	s_movk_i32 s11, 0x200
	v_sub_f32_e32 v34, v2, v159
	v_or_b32_sdwa v2, v52, s11 dst_sel:DWORD dst_unused:UNUSED_PAD src0_sel:BYTE_0 src1_sel:DWORD
	s_mov_b32 s11, 0x15555556
	v_sub_f32_e32 v36, v4, v159
	v_sub_f32_e32 v35, v3, v159
	v_mul_hi_u32 v4, v2, s11
	v_mov_b64_e32 v[2:3], s[4:5]
	s_mov_b32 s11, 0xffff
	v_and_b32_e32 v18, 0x3fffffc0, v52
	v_readlane_b32 s8, v252, 28
	v_lshlrev_b32_e32 v19, 4, v41
	v_mad_u64_u32 v[2:3], s[20:21], v4, s20, v[2:3]
	v_and_b32_sdwa v4, s11, v53 dst_sel:DWORD dst_unused:UNUSED_PAD src0_sel:DWORD src1_sel:WORD_1
	v_sub_f32_e32 v22, v24, v159
	v_sub_f32_e32 v23, v25, v159
	v_sub_f32_e32 v24, v26, v159
	v_sub_f32_e32 v25, v27, v159
	v_sub_f32_e32 v26, v28, v159
	v_sub_f32_e32 v27, v29, v159
	v_sub_f32_e32 v28, v30, v159
	v_sub_f32_e32 v29, v31, v159
	v_sub_f32_e32 v30, v32, v159
	v_sub_f32_e32 v31, v33, v159
	v_lshl_add_u32 v141, v18, 2, s8
	v_lshlrev_b32_e32 v18, 3, v41
	v_and_b32_e32 v19, 0xc0, v19
	v_lshlrev_b32_e32 v20, 1, v41
	v_sub_f32_e32 v37, v5, v159
	v_lshlrev_b32_e32 v4, 1, v4
	v_mov_b32_e32 v5, v83
	v_exp_f32_e32 v222, v46
	v_exp_f32_e32 v223, v47
	v_exp_f32_e32 v233, v22
	v_exp_f32_e32 v234, v23
	v_exp_f32_e32 v235, v24
	v_exp_f32_e32 v236, v25
	v_exp_f32_e32 v237, v26
	v_exp_f32_e32 v238, v27
	v_exp_f32_e32 v239, v28
	v_exp_f32_e32 v240, v29
	v_exp_f32_e32 v241, v30
	v_exp_f32_e32 v246, v31
	v_and_or_b32 v19, v18, 24, v19
	v_and_b32_e32 v20, 32, v20
	v_and_b32_e32 v18, 0x100, v18
	v_lshl_add_u64 v[142:143], v[2:3], 0, v[4:5]
	v_lshl_add_u64 v[2:3], s[4:5], 0, v[68:69]
	v_and_b32_e32 v4, 7, v52
	v_or3_b32 v18, v19, v20, v18
	v_sub_f32_e32 v49, v17, v159
	v_sub_f32_e32 v48, v16, v159
	s_waitcnt vmcnt(3)
	v_lshl_add_u64 v[144:145], v[2:3], 0, v[70:71]
	v_lshl_add_u64 v[2:3], s[6:7], 0, v[50:51]
	v_lshlrev_b32_e32 v4, 4, v4
	v_mov_b32_e32 v16, v83
	v_mov_b32_e32 v17, v83
	v_add_u32_e32 v158, 0, v18
	v_sub_f32_e32 v47, v15, v159
	v_sub_f32_e32 v46, v14, v159
	v_sub_f32_e32 v45, v13, v159
	v_sub_f32_e32 v44, v12, v159
	v_sub_f32_e32 v43, v11, v159
	v_sub_f32_e32 v42, v10, v159
	v_sub_f32_e32 v41, v9, v159
	v_sub_f32_e32 v40, v8, v159
	v_sub_f32_e32 v39, v7, v159
	v_sub_f32_e32 v38, v6, v159
	v_lshl_add_u64 v[146:147], v[2:3], 0, v[4:5]
	v_mov_b32_e32 v2, v83
	v_mov_b32_e32 v3, v83
	v_mov_b32_e32 v4, v83
	v_mov_b32_e32 v6, v83
	v_mov_b32_e32 v7, v83
	v_mov_b32_e32 v8, v83
	v_mov_b32_e32 v9, v83
	v_mov_b32_e32 v10, v83
	v_mov_b32_e32 v11, v83
	v_mov_b32_e32 v12, v83
	v_mov_b32_e32 v13, v83
	v_mov_b32_e32 v14, v83
	v_mov_b32_e32 v15, v83
	v_mov_b64_e32 v[32:33], v[16:17]
	s_ashr_i32 s3, s2, 31
	s_mov_b32 s22, 2
	s_mov_b32 s8, 4
	s_mov_b32 s10, 1
	s_mov_b32 s9, 0
	v_lshl_add_u32 v156, v139, 2, v141
	v_mov_b32_e32 v157, 0
	v_mov_b32_e32 v169, 1.0
	v_mov_b64_e32 v[30:31], v[14:15]
	v_mov_b64_e32 v[28:29], v[12:13]
	v_mov_b64_e32 v[26:27], v[10:11]
	v_mov_b64_e32 v[24:25], v[8:9]
	v_mov_b64_e32 v[22:23], v[6:7]
	v_mov_b64_e32 v[20:21], v[4:5]
	v_mov_b64_e32 v[18:19], v[2:3]
	s_waitcnt vmcnt(5)
	ds_write_b128 v165, v[56:59] offset:8192
	s_waitcnt vmcnt(4)
	ds_write_b128 v54, v[60:63] offset:40960
	s_waitcnt vmcnt(3)
	ds_write_b128 v55, v[64:67] offset:40960
	s_waitcnt lgkmcnt(0)
	s_barrier
	v_subrev_u32_e32 v142, s4, v142
	v_subrev_u32_e32 v144, s4, v144
	v_subrev_u32_e32 v146, s6, v146
	s_add_u32 s82, s14, s4
	s_addc_u32 s83, s15, s5
	s_add_u32 s82, s82, 0x9000
	s_addc_u32 s83, s83, 0
	s_add_u32 s84, s16, s6
	s_addc_u32 s85, s17, s7
	s_add_u32 s84, s84, 0x6000
	s_addc_u32 s85, s85, 0
	s_nop 0
	s_nop 0
	s_nop 0
	s_nop 0
	s_nop 0
	s_nop 0
	s_nop 0
	s_nop 0
	s_nop 0
	s_nop 0
	s_nop 0
	s_nop 0
	s_nop 0
	s_mov_b32 s81, 0x41380000
	v_xor_b32_e32 v188, 0x80000000, v159
	v_mov_b32_e32 v189, v188
	v_mov_b32_e32 v190, v188
	v_mov_b32_e32 v191, v188
	v_mov_b32_e32 v192, v188
	v_mov_b32_e32 v193, v188
	v_mov_b32_e32 v194, v188
	v_mov_b32_e32 v195, v188
	v_mov_b32_e32 v196, v188
	v_mov_b32_e32 v197, v188
	v_mov_b32_e32 v198, v188
	v_mov_b32_e32 v199, v188
	v_mov_b32_e32 v200, v188
	v_mov_b32_e32 v201, v188
	v_mov_b32_e32 v202, v188
	v_mov_b32_e32 v203, v188
.LBB0_1429:
	s_mov_b32 s4, s9
	s_mov_b32 s9, s22
	s_lshl_b32 s5, s10, 14
	s_add_i32 s5, s5, 0
	v_add_u32_e32 v54, s5, v167
	ds_read_b128 v[50:53], v54 offset:24576
	ds_read_b128 v[54:57], v54 offset:32768
	v_add_u32_e32 v148, s5, v168
	ds_read_b128 v[170:173], v148 offset:24576
	ds_read_b128 v[174:177], v148 offset:32768
	v_add_u32_e32 v148, s5, v166
	s_waitcnt lgkmcnt(3)
	v_mfma_f32_32x32x16_bf16 v[66:81], v[50:53], v[106:109], v[188:203]
	v_exp_f32_e32 v178, v42
	v_exp_f32_e32 v179, v43
	v_exp_f32_e32 v180, v44
	v_add_f32_e32 v143, v222, v227
	s_waitcnt lgkmcnt(2)
	v_mfma_f32_32x32x16_bf16 v[50:65], v[54:57], v[106:109], v[188:203]
	v_exp_f32_e32 v181, v45
	v_exp_f32_e32 v182, v46
	v_exp_f32_e32 v183, v47
	v_add_f32_e32 v145, v223, v230
	s_waitcnt lgkmcnt(1)
	v_mfma_f32_32x32x16_bf16 v[66:81], v[170:173], v[102:105], v[66:81]
	v_exp_f32_e32 v184, v48
	v_exp_f32_e32 v49, v49
	v_exp_f32_e32 v153, v35
	v_add_f32_e32 v143, v231, v143
	s_waitcnt lgkmcnt(0)
	v_mfma_f32_32x32x16_bf16 v[50:65], v[174:177], v[102:105], v[50:65]
	v_exp_f32_e32 v185, v34
	v_exp_f32_e32 v186, v36
	v_exp_f32_e32 v187, v37
	v_add_f32_e32 v145, v232, v145
	ds_read_b128 v[170:173], v148 offset:24576
	ds_read_b128 v[174:177], v148 offset:32768
	v_add_u32_e32 v148, s5, v162
	s_waitcnt lgkmcnt(1)
	v_mfma_f32_32x32x16_bf16 v[66:81], v[170:173], v[98:101], v[66:81]
	v_exp_f32_e32 v147, v38
	v_exp_f32_e32 v152, v39
	v_exp_f32_e32 v204, v40
	v_add_f32_e32 v143, v233, v143
	s_waitcnt lgkmcnt(0)
	v_mfma_f32_32x32x16_bf16 v[50:65], v[174:177], v[98:101], v[50:65]
	v_exp_f32_e32 v205, v41
	v_add_f32_e32 v145, v234, v145
	v_add_f32_e32 v143, v235, v143
	v_add_f32_e32 v145, v236, v145
	v_add_f32_e32 v143, v237, v143
	v_add_f32_e32 v145, v238, v145
	ds_read_b128 v[170:173], v148 offset:24576
	ds_read_b128 v[174:177], v148 offset:32768
	v_add_u32_e32 v148, s5, v161
	s_waitcnt lgkmcnt(1)
	v_mfma_f32_32x32x16_bf16 v[66:81], v[170:173], v[94:97], v[66:81]
	v_add_f32_e32 v143, v239, v143
	v_add_f32_e32 v145, v240, v145
	v_add_f32_e32 v143, v241, v143
	v_add_f32_e32 v145, v246, v145
	v_add_f32_e32 v143, v185, v143
	v_add_f32_e32 v145, v153, v145
	v_add_f32_e32 v143, v186, v143
	s_waitcnt lgkmcnt(0)
	v_mfma_f32_32x32x16_bf16 v[50:65], v[174:177], v[94:97], v[50:65]
	v_add_f32_e32 v145, v187, v145
	v_add_f32_e32 v143, v147, v143
	v_add_f32_e32 v145, v152, v145
	v_add_f32_e32 v143, v204, v143
	v_add_f32_e32 v145, v205, v145
	v_add_f32_e32 v143, v178, v143
	v_add_f32_e32 v145, v179, v145
	ds_read_b128 v[170:173], v148 offset:24576
	ds_read_b128 v[174:177], v148 offset:32768
	v_add_u32_e32 v148, s5, v160
	v_lshl_add_u32 v247, s4, 13, v158
	ds_read_b64_tr_b16 v[206:207], v247 offset:0
	ds_read_b64_tr_b16 v[208:209], v247 offset:0x400
	ds_read_b64_tr_b16 v[210:211], v247 offset:0x800
	ds_read_b64_tr_b16 v[212:213], v247 offset:0xc00
	ds_read_b64_tr_b16 v[214:215], v247 offset:0x1000
	ds_read_b64_tr_b16 v[216:217], v247 offset:0x1400
	ds_read_b64_tr_b16 v[218:219], v247 offset:0x1800
	ds_read_b64_tr_b16 v[220:221], v247 offset:0x1c00
	s_waitcnt lgkmcnt(9)
	v_mfma_f32_32x32x16_bf16 v[66:81], v[170:173], v[90:93], v[66:81]
	v_add_f32_e32 v143, v180, v143
	v_add_f32_e32 v145, v181, v145
	v_add_f32_e32 v143, v182, v143
	v_add_f32_e32 v145, v183, v145
	v_add_f32_e32 v143, v184, v143
	v_add_f32_e32 v145, v49, v145
	v_cvt_pk_bf16_f32 v34, v222, v223
	s_waitcnt lgkmcnt(8)
	v_mfma_f32_32x32x16_bf16 v[50:65], v[174:177], v[90:93], v[50:65]
	v_cvt_pk_bf16_f32 v35, v227, v230
	v_cvt_pk_bf16_f32 v36, v231, v232
	v_cvt_pk_bf16_f32 v37, v233, v234
	v_cvt_pk_bf16_f32 v38, v235, v236
	v_cvt_pk_bf16_f32 v39, v237, v238
	v_cvt_pk_bf16_f32 v40, v239, v240
	v_cvt_pk_bf16_f32 v41, v241, v246
	ds_read_b128 v[170:173], v148 offset:24576
	ds_read_b128 v[174:177], v148 offset:32768
	s_waitcnt lgkmcnt(1)
	v_mfma_f32_32x32x16_bf16 v[66:81], v[170:173], v[86:89], v[66:81]
	v_cvt_pk_bf16_f32 v42, v185, v153
	v_cvt_pk_bf16_f32 v43, v186, v187
	v_cvt_pk_bf16_f32 v44, v147, v152
	v_cvt_pk_bf16_f32 v45, v204, v205
	v_cvt_pk_bf16_f32 v46, v178, v179
	v_cvt_pk_bf16_f32 v47, v180, v181
	v_cvt_pk_bf16_f32 v48, v182, v183
	s_waitcnt lgkmcnt(0)
	v_mfma_f32_32x32x16_bf16 v[50:65], v[174:177], v[86:89], v[50:65]
	v_cvt_pk_bf16_f32 v49, v184, v49
	v_add_f32_e32 v170, v143, v145
	global_load_dwordx4 v[130:133], v146, s[84:85]
	global_load_dwordx4 v[126:129], v144, s[82:83]
	global_load_dwordx4 v[134:137], v142, s[82:83]
	s_add_u32 s82, s82, 0x3000
	s_addc_u32 s83, s83, 0
	s_add_u32 s84, s84, 0x2000
	s_addc_u32 s85, s85, 0
	s_waitcnt lgkmcnt(0)
	s_nop 0
	v_mfma_f32_32x32x16_bf16 v[2:17], v[34:37], v[206:209], v[2:17]
	ds_read_b64_tr_b16 v[172:173], v247 offset:0x200
	ds_read_b64_tr_b16 v[174:175], v247 offset:0x600
	v_max_f32_e32 v249, v67, v67
	v_max_f32_e32 v248, v66, v66
	v_max_f32_e32 v248, v248, v249
	v_max3_f32 v248, v248, v68, v69
	v_exp_f32_e32 v222, v66
	v_mfma_f32_32x32x16_bf16 v[2:17], v[38:41], v[210:213], v[2:17]
	ds_read_b64_tr_b16 v[176:177], v247 offset:0xa00
	ds_read_b64_tr_b16 v[178:179], v247 offset:0xe00
	v_max3_f32 v248, v248, v70, v71
	v_max3_f32 v248, v248, v72, v73
	v_max3_f32 v248, v248, v74, v75
	v_exp_f32_e32 v223, v67
	v_exp_f32_e32 v227, v68
	v_mfma_f32_32x32x16_bf16 v[2:17], v[42:45], v[214:217], v[2:17]
	ds_read_b64_tr_b16 v[180:181], v247 offset:0x1200
	ds_read_b64_tr_b16 v[182:183], v247 offset:0x1600
	v_max3_f32 v248, v248, v76, v77
	v_max3_f32 v248, v248, v78, v79
	v_max3_f32 v248, v248, v80, v81
	v_exp_f32_e32 v230, v69
	v_exp_f32_e32 v231, v70
	v_mfma_f32_32x32x16_bf16 v[2:17], v[46:49], v[218:221], v[2:17]
	ds_read_b64_tr_b16 v[184:185], v247 offset:0x1a00
	ds_read_b64_tr_b16 v[186:187], v247 offset:0x1e00
	v_max3_f32 v248, v248, v50, v51
	v_max3_f32 v248, v248, v52, v53
	v_max3_f32 v248, v248, v54, v55
	v_exp_f32_e32 v232, v71
	v_exp_f32_e32 v233, v72
	s_lshl_b32 s11, s9, 13
	s_lshl_b32 s4, s9, 14
	s_add_i32 s6, s4, 0
	s_waitcnt vmcnt(3)
	v_add_u32_e32 v247, s11, v165
	ds_write_b128 v247, v[114:117]
	v_add_u32_e32 v247, s6, v163
	ds_write_b128 v247, v[118:121] offset:24576
	v_add_u32_e32 v247, s6, v164
	ds_write_b128 v247, v[122:125] offset:24576
	s_waitcnt lgkmcnt(3)
	v_mfma_f32_32x32x16_bf16 v[18:33], v[34:37], v[172:175], v[18:33]
	v_max3_f32 v248, v248, v56, v57
	v_max3_f32 v248, v248, v58, v59
	v_max3_f32 v248, v248, v60, v61
	v_exp_f32_e32 v234, v73
	v_exp_f32_e32 v235, v74
	v_mfma_f32_32x32x16_bf16 v[18:33], v[38:41], v[176:179], v[18:33]
	v_max3_f32 v248, v248, v62, v63
	v_max3_f32 v248, v248, v64, v65
	v_exp_f32_e32 v236, v75
	v_exp_f32_e32 v237, v76
	v_exp_f32_e32 v238, v77
	v_mfma_f32_32x32x16_bf16 v[18:33], v[42:45], v[180:183], v[18:33]
	v_exp_f32_e32 v239, v78
	v_exp_f32_e32 v240, v79
	v_exp_f32_e32 v241, v80
	v_exp_f32_e32 v246, v81
	v_cmp_ge_f32_e32 vcc, s81, v248
	v_mfma_f32_32x32x16_bf16 v[18:33], v[46:49], v[184:187], v[18:33]
	s_cmp_eq_u64 vcc, exec
	s_cbranch_scc0 .LBB0_1448
	v_mov_b32_e32 v172, 1.0

.LBB0_1439:
	s_waitcnt lgkmcnt(0)
	s_nop 0
	v_mfma_f32_32x32x16_bf16 v[2:17], v[50:53], v[206:209], v[2:17]
	ds_read_b64_tr_b16 v[148:149], v247 offset:0x200
	ds_read_b64_tr_b16 v[150:151], v247 offset:0x600
	v_max_f32_e32 v249, v67, v67
	v_max_f32_e32 v248, v66, v66
	v_max_f32_e32 v248, v248, v249
	v_max3_f32 v248, v248, v68, v69
	v_exp_f32_e32 v222, v66
	v_mfma_f32_32x32x16_bf16 v[2:17], v[54:57], v[210:213], v[2:17]
	ds_read_b64_tr_b16 v[176:177], v247 offset:0xa00
	ds_read_b64_tr_b16 v[178:179], v247 offset:0xe00
	v_max3_f32 v248, v248, v70, v71
	v_max3_f32 v248, v248, v72, v73
	v_max3_f32 v248, v248, v74, v75
	v_exp_f32_e32 v223, v67
	v_exp_f32_e32 v227, v68
	v_mfma_f32_32x32x16_bf16 v[2:17], v[58:61], v[214:217], v[2:17]
	ds_read_b64_tr_b16 v[180:181], v247 offset:0x1200
	ds_read_b64_tr_b16 v[182:183], v247 offset:0x1600
	v_max3_f32 v248, v248, v76, v77
	v_max3_f32 v248, v248, v78, v79
	v_max3_f32 v248, v248, v80, v81
	v_exp_f32_e32 v230, v69
	v_exp_f32_e32 v231, v70
	v_mfma_f32_32x32x16_bf16 v[2:17], v[62:65], v[218:221], v[2:17]
	ds_read_b64_tr_b16 v[184:185], v247 offset:0x1a00
	ds_read_b64_tr_b16 v[186:187], v247 offset:0x1e00
	v_max3_f32 v248, v248, v34, v35
	v_max3_f32 v248, v248, v36, v37
	v_max3_f32 v248, v248, v38, v39
	v_exp_f32_e32 v232, v71
	v_exp_f32_e32 v233, v72
	s_add_i32 s6, s9, 1
	s_cmp_lg_u32 s9, 2
	s_cselect_b32 s10, s6, 0
	s_lshl_b32 s20, s10, 13
	s_lshl_b32 s6, s10, 14
	s_add_i32 s21, s6, 0
	s_waitcnt vmcnt(3)
	v_add_u32_e32 v247, s20, v165
	ds_write_b128 v247, v[130:133]
	v_add_u32_e32 v247, s21, v163
	ds_write_b128 v247, v[126:129] offset:24576
	v_add_u32_e32 v247, s21, v164
	ds_write_b128 v247, v[134:137] offset:24576
	s_waitcnt lgkmcnt(3)
	v_mfma_f32_32x32x16_bf16 v[18:33], v[50:53], v[148:151], v[18:33]
	v_max3_f32 v248, v248, v40, v41
	v_max3_f32 v248, v248, v42, v43
	v_max3_f32 v248, v248, v44, v45
	v_exp_f32_e32 v234, v73
	v_exp_f32_e32 v235, v74
	v_mfma_f32_32x32x16_bf16 v[18:33], v[54:57], v[176:179], v[18:33]
	v_max3_f32 v248, v248, v46, v47
	v_max3_f32 v248, v248, v48, v49
	v_exp_f32_e32 v236, v75
	v_exp_f32_e32 v237, v76
	v_exp_f32_e32 v238, v77
	v_mfma_f32_32x32x16_bf16 v[18:33], v[58:61], v[180:183], v[18:33]
	v_exp_f32_e32 v239, v78
	v_exp_f32_e32 v240, v79
	v_exp_f32_e32 v241, v80
	v_exp_f32_e32 v246, v81
	v_cmp_ge_f32_e32 vcc, s81, v248
	v_mfma_f32_32x32x16_bf16 v[18:33], v[62:65], v[184:187], v[18:33]
	s_cmp_eq_u64 vcc, exec
	v_mov_b32_e32 v148, 1.0
	s_cbranch_scc0 .LBB0_1449
.LBB0_1446:
	s_add_i32 s6, s10, 1
	s_cmp_lg_u32 s10, 2
	v_fmac_f32_e32 v170, v169, v157
	s_cselect_b32 s22, s6, 0
	v_fmac_f32_e32 v173, v170, v172
	v_mov_b32_e32 v157, v173
	s_add_i32 s8, s8, 2
	s_and_b64 vcc, exec, s[4:5]
	v_mov_b32_e32 v169, v148
	s_waitcnt lgkmcnt(0)
	s_barrier
	s_cbranch_vccz .LBB0_1429
	s_branch .LBB0_1450

.LBB0_1450:
	s_nop 0
	s_nop 0
	v_mov_b32_e32 v249, v157
	s_nop 1
	v_permlane32_swap_b32_e32 v157, v249
	v_add_f32_e32 v157, v157, v249
	v_add_u32_e32 v54, s21, v167
	ds_read_b128 v[50:53], v54 offset:24576
	ds_read_b128 v[54:57], v54 offset:32768
	v_add_u32_e32 v114, s21, v168
	v_exp_f32_e32 v49, v49
	s_waitcnt lgkmcnt(1)
	v_mfma_f32_32x32x16_bf16 v[66:81], v[50:53], v[106:109], 0
	s_waitcnt lgkmcnt(0)
	v_mfma_f32_32x32x16_bf16 v[50:65], v[54:57], v[106:109], 0
	ds_read_b128 v[106:109], v114 offset:24576
	ds_read_b128 v[114:117], v114 offset:32768
	s_waitcnt lgkmcnt(1)
	v_mfma_f32_32x32x16_bf16 v[66:81], v[106:109], v[102:105], v[66:81]
	v_add_u32_e32 v106, s21, v166
	s_waitcnt lgkmcnt(0)
	v_mfma_f32_32x32x16_bf16 v[50:65], v[114:117], v[102:105], v[50:65]
	ds_read_b128 v[102:105], v106 offset:24576
	ds_read_b128 v[106:109], v106 offset:32768
	s_waitcnt lgkmcnt(1)
	v_mfma_f32_32x32x16_bf16 v[66:81], v[102:105], v[98:101], v[66:81]
	v_add_u32_e32 v102, s21, v162
	s_waitcnt lgkmcnt(0)
	v_mfma_f32_32x32x16_bf16 v[50:65], v[106:109], v[98:101], v[50:65]
	ds_read_b128 v[98:101], v102 offset:24576
	ds_read_b128 v[102:105], v102 offset:32768
	s_waitcnt lgkmcnt(1)
	v_mfma_f32_32x32x16_bf16 v[66:81], v[98:101], v[94:97], v[66:81]
	v_add_u32_e32 v98, s21, v161
	s_waitcnt lgkmcnt(0)
	v_mfma_f32_32x32x16_bf16 v[50:65], v[102:105], v[94:97], v[50:65]
	ds_read_b128 v[94:97], v98 offset:24576
	ds_read_b128 v[98:101], v98 offset:32768
	s_waitcnt lgkmcnt(1)
	v_mfma_f32_32x32x16_bf16 v[66:81], v[94:97], v[90:93], v[66:81]
	v_add_u32_e32 v94, s21, v160
	s_waitcnt lgkmcnt(0)
	v_mfma_f32_32x32x16_bf16 v[50:65], v[98:101], v[90:93], v[50:65]
	ds_read_b128 v[90:93], v94 offset:24576
	ds_read_b128 v[94:97], v94 offset:32768
	v_exp_f32_e32 v98, v47
	v_exp_f32_e32 v99, v48
	s_waitcnt lgkmcnt(1)
	v_mfma_f32_32x32x16_bf16 v[66:81], v[90:93], v[86:89], v[66:81]
	v_exp_f32_e32 v90, v39
	v_exp_f32_e32 v91, v40
	v_exp_f32_e32 v92, v41
	v_exp_f32_e32 v93, v42
	s_waitcnt lgkmcnt(0)
	v_mfma_f32_32x32x16_bf16 v[50:65], v[94:97], v[86:89], v[50:65]
	v_exp_f32_e32 v86, v35
	v_exp_f32_e32 v87, v36
	v_exp_f32_e32 v88, v37
	v_exp_f32_e32 v89, v38
	v_exp_f32_e32 v94, v43
	v_exp_f32_e32 v95, v44
	v_exp_f32_e32 v96, v45
	v_mfma_f32_32x32x16_bf16 v[66:81], v[82:85], v[110:113], v[66:81]
	v_exp_f32_e32 v97, v46
	v_mfma_f32_32x32x16_bf16 v[50:65], v[82:85], v[110:113], v[50:65]
	v_exp_f32_e32 v85, v34
	v_add_f32_e32 v34, 0, v222
	v_add_f32_e32 v34, v223, v34
	v_add_f32_e32 v34, v227, v34
	v_add_f32_e32 v34, v230, v34
	v_add_f32_e32 v34, v231, v34
	v_add_f32_e32 v34, v232, v34
	v_add_f32_e32 v34, v233, v34
	v_add_f32_e32 v34, v234, v34
	v_add_f32_e32 v34, v235, v34
	v_add_f32_e32 v34, v236, v34
	v_add_f32_e32 v34, v237, v34
	v_add_f32_e32 v34, v238, v34
	v_add_f32_e32 v34, v239, v34
	v_add_f32_e32 v34, v240, v34
	v_add_f32_e32 v34, v241, v34
	v_add_f32_e32 v34, v246, v34
	v_add_f32_e32 v34, v85, v34
	v_add_f32_e32 v34, v86, v34
	v_add_f32_e32 v34, v87, v34
	v_add_f32_e32 v34, v88, v34
	v_add_f32_e32 v34, v89, v34
	v_add_f32_e32 v34, v90, v34
	v_add_f32_e32 v34, v91, v34
	v_add_f32_e32 v34, v92, v34
	v_add_f32_e32 v34, v93, v34
	v_add_f32_e32 v34, v94, v34
	v_add_f32_e32 v34, v95, v34
	v_add_f32_e32 v34, v96, v34
	v_add_f32_e32 v34, v97, v34
	v_add_f32_e32 v34, v98, v34
	v_add_f32_e32 v34, v99, v34
	v_add_f32_e32 v82, v49, v34
	v_mov_b32_e32 v84, v82
	v_cvt_pk_bf16_f32 v34, v222, v223
	v_cvt_pk_bf16_f32 v35, v227, v230
	v_cvt_pk_bf16_f32 v36, v231, v232
	s_nop 1
	v_permlane32_swap_b32_e32 v82, v84
	v_cvt_pk_bf16_f32 v37, v233, v234
	v_cvt_pk_bf16_f32 v38, v235, v236
	v_cvt_pk_bf16_f32 v39, v237, v238
	v_cvt_pk_bf16_f32 v40, v239, v240
	v_cvt_pk_bf16_f32 v41, v241, v246
	v_cvt_pk_bf16_f32 v42, v85, v86
	v_cvt_pk_bf16_f32 v43, v87, v88
	v_cvt_pk_bf16_f32 v44, v89, v90
	v_cvt_pk_bf16_f32 v45, v91, v92
	v_cvt_pk_bf16_f32 v46, v93, v94
	v_cvt_pk_bf16_f32 v47, v95, v96
	v_cvt_pk_bf16_f32 v48, v97, v98
	v_cvt_pk_bf16_f32 v49, v99, v49
	v_add_u32_e32 v85, s11, v158
	ds_read_b64_tr_b16 v[86:87], v85 offset:0
	ds_read_b64_tr_b16 v[88:89], v85 offset:0x400
	ds_read_b64_tr_b16 v[90:91], v85 offset:0x800
	ds_read_b64_tr_b16 v[92:93], v85 offset:0xc00
	ds_read_b64_tr_b16 v[94:95], v85 offset:0x1000
	ds_read_b64_tr_b16 v[96:97], v85 offset:0x1400
	ds_read_b64_tr_b16 v[98:99], v85 offset:0x1800
	ds_read_b64_tr_b16 v[100:101], v85 offset:0x1c00
	s_waitcnt lgkmcnt(0)
	s_nop 0
	v_mfma_f32_32x32x16_bf16 v[2:17], v[34:37], v[86:89], v[2:17]
	ds_read_b64_tr_b16 v[86:87], v85 offset:0x200
	ds_read_b64_tr_b16 v[88:89], v85 offset:0x600
	v_mfma_f32_32x32x16_bf16 v[2:17], v[38:41], v[90:93], v[2:17]
	ds_read_b64_tr_b16 v[90:91], v85 offset:0xa00
	ds_read_b64_tr_b16 v[92:93], v85 offset:0xe00
	v_mfma_f32_32x32x16_bf16 v[2:17], v[42:45], v[94:97], v[2:17]
	ds_read_b64_tr_b16 v[94:95], v85 offset:0x1200
	ds_read_b64_tr_b16 v[96:97], v85 offset:0x1600
	v_mfma_f32_32x32x16_bf16 v[2:17], v[46:49], v[98:101], v[2:17]
	ds_read_b64_tr_b16 v[98:99], v85 offset:0x1a00
	ds_read_b64_tr_b16 v[100:101], v85 offset:0x1e00
	s_waitcnt lgkmcnt(0)
	v_mfma_f32_32x32x16_bf16 v[18:33], v[34:37], v[86:89], v[18:33]
	v_max_f32_e32 v34, v67, v67
	v_max_f32_e32 v35, v66, v66
	v_max_f32_e32 v34, v35, v34
	v_max3_f32 v34, v34, v68, v69
	v_max3_f32 v34, v34, v70, v71
	v_max3_f32 v34, v34, v72, v73
	v_max3_f32 v34, v34, v74, v75
	v_mfma_f32_32x32x16_bf16 v[18:33], v[38:41], v[90:93], v[18:33]
	v_max3_f32 v34, v34, v76, v77
	v_max3_f32 v34, v34, v78, v79
	v_max3_f32 v34, v34, v80, v81
	v_max3_f32 v34, v34, v50, v51
	v_max3_f32 v34, v34, v52, v53
	v_max3_f32 v34, v34, v54, v55
	v_max3_f32 v34, v34, v56, v57
	v_mfma_f32_32x32x16_bf16 v[18:33], v[42:45], v[94:97], v[18:33]
	v_max3_f32 v34, v34, v58, v59
	v_max3_f32 v34, v34, v60, v61
	v_max3_f32 v34, v34, v62, v63
	v_max3_f32 v34, v34, v64, v65
	v_mov_b32_e32 v35, v34
	s_nop 1
	v_permlane32_swap_b32_e32 v34, v35
	v_mfma_f32_32x32x16_bf16 v[18:33], v[46:49], v[98:101], v[18:33]
	v_max_f32_e32 v35, v35, v35
	v_max_f32_e32 v34, v34, v34
	v_max_f32_e32 v34, v34, v35
	s_mov_b32 s4, 0x41380000
	v_cmp_ge_f32_e32 vcc, s4, v34
	s_cmp_eq_u64 vcc, exec
	v_mov_b32_e32 v85, 1.0
	s_cbranch_scc0 .LBB0_1462
	v_cmp_gt_f32_e32 vcc, 1.0, v85
	s_cbranch_vccz .LBB0_1457
